# out-proj GEMM of the fused tile chain: each workgroup starts its 4 column tiles at tile (c>>3)&3 so the workgroups are not all on the same column tile at once
# speedup vs baseline: 1.0085x; 1.0081x over previous
; #define LAS __attribute__((address_space(3)))
; #define PG8_STAGE(bufoff, gbase, voff) do { _Pragma("unroll") for (int _i = 0; _i < 2; ++_i) \
;         __builtin_amdgcn_global_load_lds((const unsigned*)((const char*)(gbase) + (voff)[_i]), (LAS unsigned*)(lds + (bufoff) + ldsw + _i * 8192), 16, 0, 0); } while (0)
; #define PG8_STAGEA(bufoff, uptr, koff, NEXT, h) do { if constexpr (GATHER) { if (NEXT) { const u32x2 _t = *(const LAS u32x2*)(vnslot + 2 * (h)); unsigned _v[2] = {_t.x, _t.y}; PG8_STAGE(bufoff, Abase + (koff), _v); } else { PG8_STAGE(bufoff, Abase + (koff), vc[h]); } } \
;         else { PG8_STAGE(bufoff, (uptr) + (size_t)(h) * hstep + (koff), voffA); } } while (0)
; #define PG8_WAIT_V(n) asm volatile("s_waitcnt vmcnt(" #n ")" ::: "memory")
;     ...
;     for (int i = 0; i < 2; ++i) { int R, C; stage_rc(tid * 16 + i * 8192, R, C); Rr[i] = R; Cc[i] = C; const int Rb = Epi::PERM ? (64 * (R >> 5) + 16 * ((R >> 2) & 3) + 4 * ((R >> 4) & 1) + (R & 3)) : R; voffB[i] = (unsigned)(Rb * rowbytes + C * 2); voffA[i] = (unsigned)(R * rowbytes + C * 2); }
;     constexpr bool GATHER = Sched::GATHER;
;     const size_t kstep = (size_t)128;
;     const size_t hstep = (size_t)HALF * rowbytes;
;     const size_t bhstep = (size_t)(Epi::PERM ? 8 : HALF) * rowbytes;
;     const unsigned ldsw = (unsigned)wid * 1024u;
;     const int aoff = lds_byte(wr * 64 + fr, fq * 8);
;     const int boff = lds_byte(wc * 32 + fr, fq * 8);
;     ...
;     Unit cur, nxt; int ui = 0; bool fresh_cur = true;
;     if (!S.next(0, cur)) return;
;     f32x4 acc[2][2][4][2];
;     union Frag { bf16x8 q[2]; i32x8 w; };
;     Frag At[4], B0[2], B1[2];
;     unsigned vc[2][2];
;     LAS unsigned* vnslot = (LAS unsigned*)(lds + (VN_OFF - 0)) + tid * 4;
;     if constexpr (GATHER) S.avoff(cur, Rr, Cc, vc, tid);
;     LAS unsigned* rowtab = (LAS unsigned*)(lds + ROWTAB_OFF);
;     if constexpr (GATHER) S.rowtab(cur, rowtab, tid);
;     const char* cB = cur.B; const char* cA = Abase + S.aoff(cur);
;     PG8_STAGE(PG8_SB(0, 0), cB, voffB); PG8_STAGE(PG8_SB(0, 1), cB + bhstep, voffB); PG8_STAGEA(PG8_SA(0, 0), cA, 0, false, 0); PG8_STAGEA(PG8_SA(0, 1), cA, 0, false, 1);
;     if (wr == 1) PG8_BAR;
;     PG8_WAIT_V(2); PG8_BAR;
;     PG8_STAGE(PG8_SB(1, 0), cB + kstep, voffB); PG8_STAGEA(PG8_SA(1, 0), cA, kstep, false, 0); PG8_STAGE(PG8_SB(1, 1), cB + bhstep + kstep, voffB);
.LBB0_400:
	v_mov_b32_e32 v6, v160
	v_readlane_b32 s8, v252, 10
	v_lshlrev_b32_e32 v4, 4, v6
	v_add_u32_e32 v1, 0x2000, v4
	v_ashrrev_i32_e32 v0, 31, v1
	v_lshrrev_b32_e32 v0, 22, v0
	v_add_u32_e32 v0, v1, v0
	v_ashrrev_i32_e32 v0, 10, v0
	v_lshlrev_b32_e32 v2, 5, v0
	v_and_b32_e32 v3, 32, v2
	v_mul_i32_i24_e32 v2, 0x400, v0
	v_sub_u32_e32 v1, v1, v2
	v_lshrrev_b32_e32 v2, 4, v1
	v_bitop3_b32 v2, v2, v1, 32 bitop3:0x6c
	v_ashrrev_i32_e32 v1, 31, v2
	v_lshrrev_b32_e32 v1, 26, v1
	v_add_u32_e32 v5, v2, v1
	v_ashrrev_i32_e32 v1, 6, v5
	v_and_b32_e32 v5, 0xc0, v5
	v_sub_u32_e32 v2, v2, v5
	v_ashrrev_i16_sdwa v2, v203, sext(v2) dst_sel:DWORD dst_unused:UNUSED_PAD src0_sel:DWORD src1_sel:BYTE_0
	v_lshlrev_b32_e32 v5, 3, v0
	v_bfe_i32 v2, v2, 0, 16
	v_and_b32_e32 v5, -16, v5
	v_add_lshl_u32 v3, v3, v2, 1
	v_add_u32_e32 v5, v1, v5
	v_lshl_add_u32 v162, v5, 10, v3
	v_lshlrev_b32_e32 v7, 2, v5
	v_and_b32_e32 v8, 3, v1
	v_lshlrev_b32_e32 v9, 1, v5
	v_lshrrev_b32_e32 v5, 2, v5
	v_and_b32_e32 v9, 0x3fffc0, v9
	v_and_b32_e32 v5, 4, v5
	v_and_or_b32 v7, v7, 48, v8
	v_or3_b32 v5, v7, v9, v5
	v_lshl_add_u32 v164, v5, 10, v3
	v_ashrrev_i32_e32 v3, 31, v6
	v_lshrrev_b32_e32 v3, 26, v3
	v_add_u32_e32 v3, v6, v3
	v_ashrrev_i32_e32 v3, 6, v3
	v_lshlrev_b32_e32 v5, 5, v3
	v_and_b32_e32 v7, 32, v5
	v_bfe_i32 v5, v6, 27, 1
	v_lshrrev_b32_e32 v5, 22, v5
	v_add_u32_e32 v5, v4, v5
	v_and_b32_e32 v5, 0xfffffc00, v5
	v_sub_u32_e32 v4, v4, v5
	v_lshrrev_b32_e32 v5, 4, v4
	v_bitop3_b32 v5, v5, v4, 32 bitop3:0x6c
	v_ashrrev_i32_e32 v4, 31, v5
	v_lshrrev_b32_e32 v4, 26, v4
	v_add_u32_e32 v8, v5, v4
	v_ashrrev_i32_e32 v4, 6, v8
	v_and_b32_e32 v8, 0xc0, v8
	v_sub_u32_e32 v5, v5, v8
	v_ashrrev_i16_sdwa v5, v203, sext(v5) dst_sel:DWORD dst_unused:UNUSED_PAD src0_sel:DWORD src1_sel:BYTE_0
	v_lshlrev_b32_e32 v8, 3, v3
	v_bfe_i32 v5, v5, 0, 16
	v_and_b32_e32 v8, -16, v8
	v_readfirstlane_b32 s5, v6
	v_add_lshl_u32 v7, v7, v5, 1
	v_add_u32_e32 v8, v4, v8
	s_ashr_i32 s6, s5, 6
	v_lshl_add_u32 v166, v8, 10, v7
	v_lshlrev_b32_e32 v9, 2, v8
	v_and_b32_e32 v10, 3, v4
	v_lshlrev_b32_e32 v11, 1, v8
	v_lshrrev_b32_e32 v8, 2, v8
	s_lshl_b32 s16, s6, 10
	v_and_b32_e32 v11, 0x3fffc0, v11
	v_and_b32_e32 v8, 4, v8
	v_and_or_b32 v9, v9, 48, v10
	v_or3_b32 v8, v9, v11, v8
	s_add_i32 s56, s16, 0
	v_lshl_add_u32 v168, v8, 10, v7
	s_bfe_u32 s98, s2, 0x20003
	s_lshl_b32 s98, s98, 18
	s_add_u32 s100, s24, s98
	s_addc_u32 s101, s25, 0
	s_add_i32 m0, s56, 0x10000
	s_ashr_i32 s3, s2, 31
	global_load_lds_dwordx4 v168, s[100:101]
	s_add_i32 m0, s56, 0x12000
	v_readlane_b32 s9, v252, 11
	global_load_lds_dwordx4 v164, s[100:101]
	s_add_i32 m0, s56, 0x14000
	s_ashr_i32 s4, s5, 8
	s_lshl_b64 s[94:95], s[2:3], 18
	s_add_u32 s8, s8, s98
	s_addc_u32 s9, s9, 0
	global_load_lds_dwordx4 v168, s[8:9]
	s_add_i32 m0, s56, 0x16000
	s_add_u32 s96, s89, s94
	s_addc_u32 s97, s33, s95
	s_add_i32 s57, s56, 0x2000
	global_load_lds_dwordx4 v164, s[8:9]
	s_mov_b32 m0, s56
	s_add_u32 s8, s96, 0x20000
	global_load_lds_dwordx4 v166, s[96:97]
	s_mov_b32 m0, s57
	s_addc_u32 s9, s97, 0
	s_add_i32 s60, s56, 0x4000
	global_load_lds_dwordx4 v162, s[96:97]
	s_mov_b32 m0, s60
	s_add_i32 s61, s56, 0x6000
	global_load_lds_dwordx4 v166, s[8:9]
	s_mov_b32 m0, s61
	s_cmp_eq_u32 s4, 1
	global_load_lds_dwordx4 v162, s[8:9]
	s_cselect_b64 s[10:11], -1, 0
	s_cmp_lg_u32 s4, 1
	s_cbranch_scc1 .LBB0_402
	s_barrier
; #define PG8_STAGE(bufoff, gbase, voff) do { _Pragma("unroll") for (int _i = 0; _i < 2; ++_i) \
;         __builtin_amdgcn_global_load_lds((const unsigned*)((const char*)(gbase) + (voff)[_i]), (LAS unsigned*)(lds + (bufoff) + ldsw + _i * 8192), 16, 0, 0); } while (0)
; #define PG8_STAGEA(bufoff, uptr, koff, NEXT, h) do { if constexpr (GATHER) { if (NEXT) { const u32x2 _t = *(const LAS u32x2*)(vnslot + 2 * (h)); unsigned _v[2] = {_t.x, _t.y}; PG8_STAGE(bufoff, Abase + (koff), _v); } else { PG8_STAGE(bufoff, Abase + (koff), vc[h]); } } \
;         else { PG8_STAGE(bufoff, (uptr) + (size_t)(h) * hstep + (koff), voffA); } } while (0)
; #define PG8_WAIT_V(n) asm volatile("s_waitcnt vmcnt(" #n ")" ::: "memory")
; #define PG8_BAR __builtin_amdgcn_s_barrier()
;     ...
;     if (wr == 1) PG8_BAR;
;     PG8_WAIT_V(2); PG8_BAR;
;     PG8_STAGE(PG8_SB(1, 0), cB + kstep, voffB); PG8_STAGEA(PG8_SA(1, 0), cA, kstep, false, 0); PG8_STAGE(PG8_SB(1, 1), cB + bhstep + kstep, voffB);
;     PG8_WAIT_V(6); PG8_BAR;
;     asm volatile("" ::: "memory");
; #pragma unroll
;     for (int a = 0; a < 2; ++a)
; #pragma unroll
;         for (int b = 0; b < 2; ++b)
; #pragma unroll
;             for (int m = 0; m < 4; ++m)
; #pragma unroll
;                 for (int n = 0; n < 2; ++n) { acc[a][b][m][n] = (f32x4){0.f, 0.f, 0.f, 0.f}; asm volatile("" : "+v"(acc[a][b][m][n])); }
;     asm volatile("s_nop 4" ::: "memory");
.LBB0_402:
	v_and_b32_e32 v7, 48, v6
	v_lshlrev_b32_e32 v12, 6, v6
	s_movk_i32 s8, 0x3c0
	v_lshlrev_b32_e32 v6, 2, v6
	s_and_b32 s6, s6, 3
	s_lshl_b32 s7, s4, 13
	v_and_or_b32 v7, v12, s8, v7
	v_and_b32_e32 v6, 32, v6
	v_readlane_b32 s8, v252, 28
	v_mov_b32_e32 v169, v24
	v_bitop3_b32 v12, v7, s7, v6 bitop3:0xde
	s_lshl_b32 s7, s6, 12
	v_readlane_b32 s9, v252, 29
	s_add_u32 s8, s8, s98
	s_addc_u32 s9, s9, 0
	v_mov_b32_e32 v165, v24
	v_mov_b32_e32 v167, v24
	v_bitop3_b32 v184, v7, s7, v6 bitop3:0xde
	s_add_i32 m0, s56, 0x18000
	v_lshl_add_u64 v[6:7], s[8:9], 0, v[168:169]
	v_lshl_add_u64 v[8:9], s[96:97], 0, v[166:167]
	v_mov_b32_e32 v163, v24
	s_waitcnt vmcnt(2)
	s_barrier
	global_load_lds_dwordx4 v[6:7], off
	v_lshl_add_u64 v[6:7], s[8:9], 0, v[164:165]
	s_add_i32 m0, s56, 0x1a000
	s_add_i32 s62, s56, 0x8000
	v_lshl_add_u64 v[10:11], s[96:97], 0, v[162:163]
	global_load_lds_dwordx4 v[6:7], off
	v_lshl_add_u64 v[6:7], v[8:9], 0, s[82:83]
	s_mov_b32 m0, s62
	s_add_i32 s63, s56, 0xa000
	v_readlane_b32 s8, v252, 30
	global_load_lds_dwordx4 v[6:7], off
	v_lshl_add_u64 v[6:7], v[10:11], 0, s[82:83]
	s_mov_b32 m0, s63
	v_readlane_b32 s9, v252, 31
	s_add_u32 s8, s8, s98
	s_addc_u32 s9, s9, 0
	global_load_lds_dwordx4 v[6:7], off
	s_add_i32 m0, s56, 0x1c000
	v_lshl_add_u64 v[6:7], s[8:9], 0, v[168:169]
	global_load_lds_dwordx4 v[6:7], off
	v_lshl_add_u64 v[6:7], s[8:9], 0, v[164:165]
	s_add_i32 m0, s56, 0x1e000
	s_mov_b32 s12, 0
	global_load_lds_dwordx4 v[6:7], off
	v_lshlrev_b32_e32 v6, 13, v3
	v_and_b32_e32 v6, 0xffffc000, v6
	v_lshl_add_u32 v4, v4, 10, v6
	v_and_b32_e32 v3, 1, v3
	s_mov_b32 s14, s12
	s_mov_b32 s15, s12
	v_lshl_or_b32 v3, v3, 6, v4
	s_mov_b32 s13, s12
	v_mov_b64_e32 v[34:35], s[14:15]
	v_mov_b64_e32 v[154:155], s[14:15]
	v_mov_b64_e32 v[146:147], s[14:15]
	v_mov_b64_e32 v[138:139], s[14:15]
	v_mov_b64_e32 v[130:131], s[14:15]
	v_mov_b64_e32 v[122:123], s[14:15]
	v_mov_b64_e32 v[114:115], s[14:15]
	v_mov_b64_e32 v[106:107], s[14:15]
	v_mov_b64_e32 v[98:99], s[14:15]
	v_mov_b64_e32 v[158:159], s[14:15]
	v_mov_b64_e32 v[150:151], s[14:15]
	v_mov_b64_e32 v[142:143], s[14:15]
	v_mov_b64_e32 v[134:135], s[14:15]
	v_mov_b64_e32 v[126:127], s[14:15]
	v_mov_b64_e32 v[118:119], s[14:15]
	v_mov_b64_e32 v[110:111], s[14:15]
	v_mov_b64_e32 v[102:103], s[14:15]
	v_mov_b64_e32 v[90:91], s[14:15]
	v_mov_b64_e32 v[82:83], s[14:15]
	v_mov_b64_e32 v[74:75], s[14:15]
	v_mov_b64_e32 v[66:67], s[14:15]
	v_mov_b64_e32 v[58:59], s[14:15]
	v_mov_b64_e32 v[50:51], s[14:15]
	v_mov_b64_e32 v[46:47], s[14:15]
	v_mov_b64_e32 v[42:43], s[14:15]
	v_mov_b64_e32 v[94:95], s[14:15]
	v_mov_b64_e32 v[86:87], s[14:15]
	v_mov_b64_e32 v[78:79], s[14:15]
	v_mov_b64_e32 v[70:71], s[14:15]
	v_mov_b64_e32 v[62:63], s[14:15]
	v_mov_b64_e32 v[54:55], s[14:15]
	v_mov_b64_e32 v[38:39], s[14:15]
	v_lshl_add_u32 v170, v5, 1, v3
	v_lshlrev_b32_e32 v3, 13, v0
	v_mov_b64_e32 v[32:33], s[12:13]
	v_mov_b64_e32 v[152:153], s[12:13]
	v_mov_b64_e32 v[144:145], s[12:13]
	v_mov_b64_e32 v[136:137], s[12:13]
	v_mov_b64_e32 v[128:129], s[12:13]
	v_mov_b64_e32 v[120:121], s[12:13]
	v_mov_b64_e32 v[112:113], s[12:13]
	v_mov_b64_e32 v[104:105], s[12:13]
	v_mov_b64_e32 v[96:97], s[12:13]
	v_mov_b64_e32 v[156:157], s[12:13]
	v_mov_b64_e32 v[148:149], s[12:13]
	v_mov_b64_e32 v[140:141], s[12:13]
	v_mov_b64_e32 v[132:133], s[12:13]
	v_mov_b64_e32 v[124:125], s[12:13]
	v_mov_b64_e32 v[116:117], s[12:13]
	v_mov_b64_e32 v[108:109], s[12:13]
	v_mov_b64_e32 v[100:101], s[12:13]
	v_mov_b64_e32 v[88:89], s[12:13]
	v_mov_b64_e32 v[80:81], s[12:13]
	v_mov_b64_e32 v[72:73], s[12:13]
	v_mov_b64_e32 v[64:65], s[12:13]
	v_mov_b64_e32 v[56:57], s[12:13]
	v_mov_b64_e32 v[48:49], s[12:13]
	v_mov_b64_e32 v[44:45], s[12:13]
	v_mov_b64_e32 v[40:41], s[12:13]
	v_mov_b64_e32 v[92:93], s[12:13]
	v_mov_b64_e32 v[84:85], s[12:13]
	v_mov_b64_e32 v[76:77], s[12:13]
	v_mov_b64_e32 v[68:69], s[12:13]
	v_mov_b64_e32 v[60:61], s[12:13]
	v_mov_b64_e32 v[52:53], s[12:13]
	v_mov_b64_e32 v[36:37], s[12:13]
	v_and_b32_e32 v3, 0xffffc000, v3
	s_waitcnt vmcnt(6)
	s_barrier
	s_nop 4
	v_lshl_add_u32 v1, v1, 10, v3
	v_and_b32_e32 v0, 1, v0
	s_cmpk_lt_u32 s5, 0x100
	v_lshl_or_b32 v0, v0, 6, v1
	s_cselect_b64 s[14:15], -1, 0
	v_lshl_add_u32 v185, s6, 6, v198
	v_lshl_or_b32 v186, s4, 6, v197
	v_mov_b32_e32 v171, v24
	v_lshl_add_u32 v172, v2, 1, v0
	v_mov_b32_e32 v173, v24
	v_add_u32_e32 v187, 0, v12
	s_mov_b32 s92, s2
	s_add_u32 s30, s24, s98
	s_addc_u32 s31, s25, 0
	s_mov_b32 s64, s12
	s_branch .LBB0_405

; #define LAS __attribute__((address_space(3)))
;     __device__ __forceinline__ size_t aoff(const Unit& u) const { return (size_t)u.pm * BM * K * 2; }
;     __device__ __forceinline__ bool next(int i, Unit& u) const { if (i >= ncol) return false; u.pm = pm; u.pn = i; u.B = Bt + (size_t)i * BM * K * 2; u.e = 0; u.cnt = 0; u.off = 0; return true; }
;     __device__ __forceinline__ size_t aoff(const Unit& u) const { return (size_t)u.pm * BM * K * 2; }
;     ...
;         const bool has_next = S.next(ui + 1, nxt);
;         if constexpr (GATHER) {
;             unsigned vn[2][2];
;             if (has_next) S.avoff(nxt, Rr, Cc, vn, tid);
;             else {
; #pragma unroll
;                 for (int h = 0; h < 2; ++h)
; #pragma unroll
;                     for (int i = 0; i < 2; ++i) vn[h][i] = vc[h][i];
;             }
;             *(LAS u32x4*)vnslot = (u32x4){vn[0][0], vn[0][1], vn[1][0], vn[1][1]};
;             if (has_next) S.rowtab(nxt, rowtab + 512 * ((ui + 1) % 3), tid);
;         }
;         const char* nB = has_next ? nxt.B : cB; const char* nA = has_next ? Abase + S.aoff(nxt) : cA;
;         const bool fresh_nxt = !(AREUSE && has_next && nxt.e == cur.e && nxt.pm == cur.pm);
;         const bool ff = fresh_cur && fresh_nxt;
;     ...
;         for (int t = 0; t < nt; t += 2) {
;             const bool last = (t == nt - 2);
;             const size_t k1 = (size_t)(t + 1) * kstep;
;             const size_t k2 = last ? (size_t)0 : (size_t)(t + 2) * kstep, k3 = k2 + kstep;
;             const char* u2 = last ? nA : cA; const char* b2 = last ? nB : cB + (size_t)(t + 2) * kstep;
;             const char* b3 = b2 + kstep;
.LBB0_405:
	s_mov_b32 s13, s64
	s_add_i32 s64, s64, 1
	s_cmp_lt_u32 s13, 3
	s_cselect_b64 s[8:9], -1, 0
	s_lshl_b32 s6, s64, 18
	s_add_i32 s6, s6, s98
	s_and_b32 s6, s6, 0xc0000
	s_add_u32 s20, s24, s6
	s_addc_u32 s21, s25, 0
	s_and_b64 s[6:7], s[8:9], exec
	s_mov_b64 s[4:5], s[30:31]
	s_mov_b32 s65, s92
	s_cselect_b32 s92, s2, s92
	s_cselect_b32 s31, s21, s5
	s_cselect_b32 s30, s20, s4
	s_ashr_i32 s93, s92, 31
	s_lshl_b64 s[6:7], s[92:93], 18
	s_add_u32 s20, s89, s6
	s_addc_u32 s21, s33, s7
	s_mov_b64 vcc, s[96:97]
	s_and_b64 s[6:7], s[8:9], exec
	s_cselect_b32 s97, s21, vcc_hi
	s_cselect_b32 s96, s20, vcc_lo
	s_add_u32 s93, s4, 0x100
	s_addc_u32 s66, s5, 0
	s_add_u32 s4, vcc_lo, 0x20080
	s_addc_u32 s5, vcc_hi, 0
	v_lshl_add_u64 v[26:27], s[4:5], 0, v[170:171]
	v_lshl_add_u64 v[174:175], s[4:5], 0, v[172:173]
	s_mov_b32 s67, -2
	s_mov_b64 s[6:7], 0

; #define LAS __attribute__((address_space(3)))
; __device__ __forceinline__ unsigned cvt_pk_bf16(float lo, float hi) { unsigned r; asm volatile("v_cvt_pk_bf16_f32 %0, %1, %2" : "=v"(r) : "v"(lo), "v"(hi)); return r; }
;     __device__ __forceinline__ void operator()(const f32x4 (&acc)[2][2][4][2], const Unit& u, int wr, int wc, int fr, int fq, const LAS unsigned* rt) const {
;         const int b = (u.pm * BM) >> 11; const int col0 = u.pn * BM + wc * 64 + 16 * fq;
;         f32x4 g[2][2];
; #pragma unroll
;         for (int bj = 0; bj < 2; ++bj)
; #pragma unroll
;             for (int n = 0; n < 2; ++n) g[bj][n] = *(const f32x4*)(mod + b * 6144 + MOD_GATE_A + col0 + 8 * bj + 4 * n) * INV_IN8;
; #pragma unroll
;         for (int ai = 0; ai < 2; ++ai)
; #pragma unroll
;             for (int m = 0; m < 4; ++m) { const size_t o = (size_t)(u.pm * BM + ai * HALF + wr * 64 + m * 16 + fr) * D + col0;
;                 const f32x4 x0 = *(const f32x4*)(x + o), x1 = *(const f32x4*)(x + o + 4), x2 = *(const f32x4*)(x + o + 8), x3 = *(const f32x4*)(x + o + 12);
;                 const f32x4 xs[2][2] = {{x0, x1}, {x2, x3}};
; #pragma unroll
;                 for (int bj = 0; bj < 2; ++bj) {
;                     const f32x4 t0 = xs[bj][0] * ALPHA + g[bj][0] * acc[ai][bj][m][0], t1 = xs[bj][1] * ALPHA + g[bj][1] * acc[ai][bj][m][1];
;                     u32x4 w; w.x = cvt_pk_bf16(t0[0], t0[1]); w.y = cvt_pk_bf16(t0[2], t0[3]); w.z = cvt_pk_bf16(t1[0], t1[1]); w.w = cvt_pk_bf16(t1[2], t1[3]);
;                     *(u32x4*)(tb + o + 8 * bj) = w; } }
.LBB0_409:
	s_lshl_b32 s100, s12, 18
	s_add_i32 s100, s100, s98
	s_bfe_u32 s100, s100, 0x20012
	s_lshr_b32 s4, s65, 3
	s_mulk_i32 s4, 0x1800
	s_ashr_i32 s5, s4, 31
	s_lshl_b64 s[4:5], s[4:5], 2
	v_lshl_add_u32 v16, s100, 8, v185
	s_add_u32 s4, s85, s4
	s_addc_u32 s5, s87, s5
	v_ashrrev_i32_e32 v17, 31, v16
	v_lshl_add_u64 v[0:1], v[16:17], 2, s[4:5]
	s_mov_b64 s[4:5], 0x2000
	v_lshl_add_u64 v[4:5], v[0:1], 0, s[4:5]
	v_add_co_u32_e32 v0, vcc, s41, v0
	s_nop 15
	s_nop 15
	s_nop 1
	v_addc_co_u32_e32 v1, vcc, 0, v1, vcc
	global_load_dwordx4 v[0:3], v[0:1], off
	s_nop 0
	global_load_dwordx4 v[18:21], v[4:5], off offset:48
	global_load_dwordx4 v[174:177], v[4:5], off offset:32
	s_nop 0
	global_load_dwordx4 v[4:7], v[4:5], off offset:16
	s_mov_b64 s[4:5], -1
	s_cmp_eq_u32 s13, 3
	v_lshl_add_u32 v192, s65, 8, v186
	v_ashrrev_i32_e32 v193, 31, v192
	v_lshlrev_b64 v[192:193], 10, v[192:193]
	v_lshl_add_u64 v[192:193], v[192:193], 0, v[16:17]
	v_lshl_add_u64 v[250:251], v[192:193], 2, s[18:19]
	s_mov_b32 s101, 0
	global_load_dwordx4 v[206:209], v[250:251], off offset:48
	global_load_dwordx4 v[210:213], v[250:251], off offset:32
	global_load_dwordx4 v[214:217], v[250:251], off offset:16
	global_load_dwordx4 v[218:221], v[250:251], off
	s_mov_b32 s100, 0x10000
	v_lshl_add_u64 v[234:235], v[250:251], 0, s[100:101]
	global_load_dwordx4 v[222:225], v[234:235], off offset:48
	global_load_dwordx4 v[226:229], v[234:235], off offset:32
	global_load_dwordx4 v[230:233], v[234:235], off offset:16
	s_nop 0
	global_load_dwordx4 v[234:237], v[234:235], off
	s_mov_b32 s100, 0x20000
	v_lshl_add_u64 v[192:193], v[250:251], 0, s[100:101]
	global_load_dwordx4 v[238:241], v[192:193], off offset:48
	global_load_dwordx4 v[242:245], v[192:193], off offset:32
	global_load_dwordx4 v[246:249], v[192:193], off offset:16
	s_nop 0
	global_load_dwordx4 v[192:195], v[192:193], off
	s_waitcnt vmcnt(12)
	v_pk_mul_f32 v[12:13], v[2:3], s[84:85] op_sel_hi:[1,0]
	v_pk_mul_f32 v[2:3], v[18:19], s[84:85] op_sel_hi:[1,0]
	v_lshl_add_u32 v18, s65, 8, v186
	v_ashrrev_i32_e32 v19, 31, v18
	v_pk_mul_f32 v[14:15], v[0:1], s[84:85] op_sel_hi:[1,0]
	v_pk_mul_f32 v[0:1], v[20:21], s[84:85] op_sel_hi:[1,0]
	v_lshlrev_b64 v[20:21], 10, v[18:19]
	v_lshl_add_u64 v[26:27], v[20:21], 0, v[16:17]
	v_pk_mul_f32 v[8:9], v[6:7], s[84:85] op_sel_hi:[1,0]
	v_pk_mul_f32 v[10:11], v[4:5], s[84:85] op_sel_hi:[1,0]
	v_pk_mul_f32 v[4:5], v[176:177], s[84:85] op_sel_hi:[1,0]
	v_pk_mul_f32 v[6:7], v[174:175], s[84:85] op_sel_hi:[1,0]
	v_lshl_add_u64 v[26:27], v[26:27], 1, s[50:51]
	s_waitcnt vmcnt(11)
	v_pk_mul_f32 v[22:23], v[208:209], s[86:87] op_sel_hi:[1,0]
	v_pk_mul_f32 v[20:21], v[206:207], s[86:87] op_sel_hi:[1,0]
	s_waitcnt vmcnt(9)
	v_pk_mul_f32 v[180:181], v[216:217], s[86:87] op_sel_hi:[1,0]
	v_pk_mul_f32 v[178:179], v[214:215], s[86:87] op_sel_hi:[1,0]
	s_waitcnt vmcnt(8)
	v_pk_mul_f32 v[182:183], v[220:221], s[86:87] op_sel_hi:[1,0]
	v_pk_mul_f32 v[188:189], v[218:219], s[86:87] op_sel_hi:[1,0]
	v_pk_fma_f32 v[180:181], v[146:147], v[8:9], v[180:181]
	v_pk_fma_f32 v[146:147], v[144:145], v[10:11], v[178:179]
	v_pk_fma_f32 v[154:155], v[154:155], v[12:13], v[182:183]
	v_pk_fma_f32 v[152:153], v[152:153], v[14:15], v[188:189]
	v_pk_fma_f32 v[150:151], v[150:151], v[0:1], v[22:23]
	v_cvt_pk_bf16_f32 v144, v152, v153
	v_cvt_pk_bf16_f32 v145, v154, v155
	v_cvt_pk_bf16_f32 v146, v146, v147
	v_cvt_pk_bf16_f32 v147, v180, v181
	global_store_dwordx4 v[26:27], v[144:147], off
	v_pk_fma_f32 v[22:23], v[148:149], v[2:3], v[20:21]
	s_nop 0
	v_pk_mul_f32 v[146:147], v[210:211], s[86:87] op_sel_hi:[1,0]
	v_pk_mul_f32 v[144:145], v[212:213], s[86:87] op_sel_hi:[1,0]
	v_pk_fma_f32 v[146:147], v[156:157], v[6:7], v[146:147]
	v_pk_fma_f32 v[144:145], v[158:159], v[4:5], v[144:145]
	v_cvt_pk_bf16_f32 v20, v146, v147
	s_nop 0
	v_cvt_pk_bf16_f32 v21, v144, v145
	v_cvt_pk_bf16_f32 v22, v22, v23
	v_cvt_pk_bf16_f32 v23, v150, v151
	global_store_dwordx4 v[26:27], v[20:23], off offset:16
	s_nop 1
	v_or_b32_e32 v20, 16, v18
	v_ashrrev_i32_e32 v21, 31, v20
	v_lshlrev_b64 v[20:21], 10, v[20:21]
	v_lshl_add_u64 v[26:27], v[20:21], 0, v[16:17]
	s_mov_b32 s100, 0x30000
	v_lshl_add_u64 v[218:219], v[250:251], 0, s[100:101]
	global_load_dwordx4 v[206:209], v[218:219], off offset:48
	global_load_dwordx4 v[210:213], v[218:219], off offset:32
	global_load_dwordx4 v[214:217], v[218:219], off offset:16
	s_nop 0
	global_load_dwordx4 v[218:221], v[218:219], off
	v_lshl_add_u64 v[26:27], v[26:27], 1, s[50:51]
	s_waitcnt vmcnt(13)
	v_pk_mul_f32 v[22:23], v[224:225], s[86:87] op_sel_hi:[1,0]
	v_pk_mul_f32 v[20:21], v[222:223], s[86:87] op_sel_hi:[1,0]
	s_waitcnt vmcnt(11)
	v_pk_mul_f32 v[150:151], v[232:233], s[86:87] op_sel_hi:[1,0]
	v_pk_mul_f32 v[148:149], v[230:231], s[86:87] op_sel_hi:[1,0]
	s_waitcnt vmcnt(10)
	v_pk_mul_f32 v[154:155], v[236:237], s[86:87] op_sel_hi:[1,0]
	v_pk_mul_f32 v[152:153], v[234:235], s[86:87] op_sel_hi:[1,0]
	v_pk_fma_f32 v[150:151], v[130:131], v[8:9], v[150:151]
	v_pk_fma_f32 v[130:131], v[128:129], v[10:11], v[148:149]
	v_pk_fma_f32 v[138:139], v[138:139], v[12:13], v[154:155]
	v_pk_fma_f32 v[136:137], v[136:137], v[14:15], v[152:153]
	v_pk_fma_f32 v[134:135], v[134:135], v[0:1], v[22:23]
	v_cvt_pk_bf16_f32 v128, v136, v137
	v_cvt_pk_bf16_f32 v129, v138, v139
	v_cvt_pk_bf16_f32 v130, v130, v131
	v_cvt_pk_bf16_f32 v131, v150, v151
	global_store_dwordx4 v[26:27], v[128:131], off
	v_pk_fma_f32 v[22:23], v[132:133], v[2:3], v[20:21]
	s_nop 0
	v_pk_mul_f32 v[130:131], v[226:227], s[86:87] op_sel_hi:[1,0]
	v_pk_mul_f32 v[128:129], v[228:229], s[86:87] op_sel_hi:[1,0]
	v_pk_fma_f32 v[130:131], v[140:141], v[6:7], v[130:131]
	v_pk_fma_f32 v[128:129], v[142:143], v[4:5], v[128:129]
	v_cvt_pk_bf16_f32 v20, v130, v131
	s_nop 0
	v_cvt_pk_bf16_f32 v21, v128, v129
	v_cvt_pk_bf16_f32 v22, v22, v23
	v_cvt_pk_bf16_f32 v23, v134, v135
	global_store_dwordx4 v[26:27], v[20:23], off offset:16
	s_nop 1
	v_or_b32_e32 v20, 32, v18
	v_ashrrev_i32_e32 v21, 31, v20
	v_lshlrev_b64 v[20:21], 10, v[20:21]
	v_lshl_add_u64 v[26:27], v[20:21], 0, v[16:17]
	s_mov_b32 s100, 0x80000
	v_lshl_add_u64 v[234:235], v[250:251], 0, s[100:101]
	global_load_dwordx4 v[222:225], v[234:235], off offset:48
	global_load_dwordx4 v[226:229], v[234:235], off offset:32
	global_load_dwordx4 v[230:233], v[234:235], off offset:16
	s_nop 0
	global_load_dwordx4 v[234:237], v[234:235], off
	v_lshl_add_u64 v[26:27], v[26:27], 1, s[50:51]
	s_waitcnt vmcnt(15)
; __device__ __forceinline__ unsigned cvt_pk_bf16(float lo, float hi) { unsigned r; asm volatile("v_cvt_pk_bf16_f32 %0, %1, %2" : "=v"(r) : "v"(lo), "v"(hi)); return r; }
;     __device__ __forceinline__ void operator()(const f32x4 (&acc)[2][2][4][2], const Unit& u, int wr, int wc, int fr, int fq, const LAS unsigned* rt) const {
;     ...
;         for (int ai = 0; ai < 2; ++ai)
; #pragma unroll
;             for (int m = 0; m < 4; ++m) { const size_t o = (size_t)(u.pm * BM + ai * HALF + wr * 64 + m * 16 + fr) * D + col0;
;                 const f32x4 x0 = *(const f32x4*)(x + o), x1 = *(const f32x4*)(x + o + 4), x2 = *(const f32x4*)(x + o + 8), x3 = *(const f32x4*)(x + o + 12);
;                 const f32x4 xs[2][2] = {{x0, x1}, {x2, x3}};
; #pragma unroll
;                 for (int bj = 0; bj < 2; ++bj) {
;                     const f32x4 t0 = xs[bj][0] * ALPHA + g[bj][0] * acc[ai][bj][m][0], t1 = xs[bj][1] * ALPHA + g[bj][1] * acc[ai][bj][m][1];
;                     u32x4 w; w.x = cvt_pk_bf16(t0[0], t0[1]); w.y = cvt_pk_bf16(t0[2], t0[3]); w.z = cvt_pk_bf16(t1[0], t1[1]); w.w = cvt_pk_bf16(t1[2], t1[3]);
;                     *(u32x4*)(tb + o + 8 * bj) = w; } }
	v_pk_mul_f32 v[22:23], v[240:241], s[86:87] op_sel_hi:[1,0]
	v_pk_mul_f32 v[20:21], v[238:239], s[86:87] op_sel_hi:[1,0]
	s_waitcnt vmcnt(13)
	v_pk_mul_f32 v[134:135], v[248:249], s[86:87] op_sel_hi:[1,0]
	v_pk_mul_f32 v[132:133], v[246:247], s[86:87] op_sel_hi:[1,0]
	s_waitcnt vmcnt(12)
	v_pk_mul_f32 v[138:139], v[194:195], s[86:87] op_sel_hi:[1,0]
	v_pk_mul_f32 v[136:137], v[192:193], s[86:87] op_sel_hi:[1,0]
	v_pk_fma_f32 v[134:135], v[114:115], v[8:9], v[134:135]
	v_pk_fma_f32 v[114:115], v[112:113], v[10:11], v[132:133]
	v_pk_fma_f32 v[122:123], v[122:123], v[12:13], v[138:139]
	v_pk_fma_f32 v[120:121], v[120:121], v[14:15], v[136:137]
	v_pk_fma_f32 v[118:119], v[118:119], v[0:1], v[22:23]
	v_cvt_pk_bf16_f32 v112, v120, v121
	v_cvt_pk_bf16_f32 v113, v122, v123
	v_cvt_pk_bf16_f32 v114, v114, v115
	v_cvt_pk_bf16_f32 v115, v134, v135
	global_store_dwordx4 v[26:27], v[112:115], off
	v_pk_fma_f32 v[22:23], v[116:117], v[2:3], v[20:21]
	s_nop 0
	v_pk_mul_f32 v[114:115], v[242:243], s[86:87] op_sel_hi:[1,0]
	v_pk_mul_f32 v[112:113], v[244:245], s[86:87] op_sel_hi:[1,0]
	v_pk_fma_f32 v[114:115], v[124:125], v[6:7], v[114:115]
	v_pk_fma_f32 v[112:113], v[126:127], v[4:5], v[112:113]
	v_cvt_pk_bf16_f32 v20, v114, v115
	s_nop 0
	v_cvt_pk_bf16_f32 v21, v112, v113
	v_cvt_pk_bf16_f32 v22, v22, v23
	v_cvt_pk_bf16_f32 v23, v118, v119
	global_store_dwordx4 v[26:27], v[20:23], off offset:16
	s_nop 1
	v_or_b32_e32 v20, 48, v18
	v_ashrrev_i32_e32 v21, 31, v20
	v_lshlrev_b64 v[20:21], 10, v[20:21]
	v_lshl_add_u64 v[26:27], v[20:21], 0, v[16:17]
	s_mov_b32 s100, 0x90000
	v_lshl_add_u64 v[192:193], v[250:251], 0, s[100:101]
	global_load_dwordx4 v[238:241], v[192:193], off offset:48
	global_load_dwordx4 v[242:245], v[192:193], off offset:32
	global_load_dwordx4 v[246:249], v[192:193], off offset:16
	s_nop 0
	global_load_dwordx4 v[192:195], v[192:193], off
	v_lshl_add_u64 v[26:27], v[26:27], 1, s[50:51]
	s_waitcnt vmcnt(15)
	v_pk_mul_f32 v[22:23], v[208:209], s[86:87] op_sel_hi:[1,0]
	v_pk_mul_f32 v[20:21], v[206:207], s[86:87] op_sel_hi:[1,0]
	s_waitcnt vmcnt(13)
	v_pk_mul_f32 v[118:119], v[216:217], s[86:87] op_sel_hi:[1,0]
	v_pk_mul_f32 v[116:117], v[214:215], s[86:87] op_sel_hi:[1,0]
	s_waitcnt vmcnt(12)
	v_pk_mul_f32 v[122:123], v[220:221], s[86:87] op_sel_hi:[1,0]
	v_pk_mul_f32 v[120:121], v[218:219], s[86:87] op_sel_hi:[1,0]
	v_pk_fma_f32 v[118:119], v[98:99], v[8:9], v[118:119]
	v_pk_fma_f32 v[98:99], v[96:97], v[10:11], v[116:117]
	v_pk_fma_f32 v[106:107], v[106:107], v[12:13], v[122:123]
	v_pk_fma_f32 v[104:105], v[104:105], v[14:15], v[120:121]
	v_pk_fma_f32 v[102:103], v[102:103], v[0:1], v[22:23]
	v_cvt_pk_bf16_f32 v96, v104, v105
	v_cvt_pk_bf16_f32 v97, v106, v107
	v_cvt_pk_bf16_f32 v98, v98, v99
	v_cvt_pk_bf16_f32 v99, v118, v119
	global_store_dwordx4 v[26:27], v[96:99], off
	v_pk_fma_f32 v[22:23], v[100:101], v[2:3], v[20:21]
	s_nop 0
	v_pk_mul_f32 v[98:99], v[210:211], s[86:87] op_sel_hi:[1,0]
	v_pk_mul_f32 v[96:97], v[212:213], s[86:87] op_sel_hi:[1,0]
	v_pk_fma_f32 v[98:99], v[108:109], v[6:7], v[98:99]
	v_pk_fma_f32 v[96:97], v[110:111], v[4:5], v[96:97]
	v_cvt_pk_bf16_f32 v20, v98, v99
	s_nop 0
	v_cvt_pk_bf16_f32 v21, v96, v97
	v_cvt_pk_bf16_f32 v22, v22, v23
	v_cvt_pk_bf16_f32 v23, v102, v103
	global_store_dwordx4 v[26:27], v[20:23], off offset:16
	s_nop 1
	v_add_u32_e32 v20, 0x80, v18
	v_ashrrev_i32_e32 v21, 31, v20
	v_lshlrev_b64 v[20:21], 10, v[20:21]
	v_lshl_add_u64 v[26:27], v[20:21], 0, v[16:17]
	s_mov_b32 s100, 0xa0000
	v_lshl_add_u64 v[218:219], v[250:251], 0, s[100:101]
	global_load_dwordx4 v[206:209], v[218:219], off offset:48
	global_load_dwordx4 v[210:213], v[218:219], off offset:32
	global_load_dwordx4 v[214:217], v[218:219], off offset:16
	s_nop 0
	global_load_dwordx4 v[218:221], v[218:219], off
	v_lshl_add_u64 v[26:27], v[26:27], 1, s[50:51]
	s_waitcnt vmcnt(15)
	v_pk_mul_f32 v[22:23], v[224:225], s[86:87] op_sel_hi:[1,0]
	v_pk_mul_f32 v[20:21], v[222:223], s[86:87] op_sel_hi:[1,0]
	s_waitcnt vmcnt(13)
	v_pk_mul_f32 v[102:103], v[232:233], s[86:87] op_sel_hi:[1,0]
	v_pk_mul_f32 v[100:101], v[230:231], s[86:87] op_sel_hi:[1,0]
	s_waitcnt vmcnt(12)
	v_pk_mul_f32 v[106:107], v[236:237], s[86:87] op_sel_hi:[1,0]
	v_pk_mul_f32 v[104:105], v[234:235], s[86:87] op_sel_hi:[1,0]
	v_pk_fma_f32 v[102:103], v[82:83], v[8:9], v[102:103]
	v_pk_fma_f32 v[82:83], v[80:81], v[10:11], v[100:101]
	v_pk_fma_f32 v[90:91], v[90:91], v[12:13], v[106:107]
	v_pk_fma_f32 v[88:89], v[88:89], v[14:15], v[104:105]
	v_pk_fma_f32 v[86:87], v[86:87], v[0:1], v[22:23]
	v_cvt_pk_bf16_f32 v80, v88, v89
	v_cvt_pk_bf16_f32 v81, v90, v91
	v_cvt_pk_bf16_f32 v82, v82, v83
	v_cvt_pk_bf16_f32 v83, v102, v103
	global_store_dwordx4 v[26:27], v[80:83], off
	v_pk_fma_f32 v[22:23], v[84:85], v[2:3], v[20:21]
	s_nop 0
	v_pk_mul_f32 v[82:83], v[226:227], s[86:87] op_sel_hi:[1,0]
	v_pk_mul_f32 v[80:81], v[228:229], s[86:87] op_sel_hi:[1,0]
	v_pk_fma_f32 v[82:83], v[92:93], v[6:7], v[82:83]
	v_pk_fma_f32 v[80:81], v[94:95], v[4:5], v[80:81]
	v_cvt_pk_bf16_f32 v20, v82, v83
	s_nop 0
	v_cvt_pk_bf16_f32 v21, v80, v81
	v_cvt_pk_bf16_f32 v22, v22, v23
	v_cvt_pk_bf16_f32 v23, v86, v87
	global_store_dwordx4 v[26:27], v[20:23], off offset:16
	s_nop 1
	v_add_u32_e32 v20, 0x90, v18
	v_ashrrev_i32_e32 v21, 31, v20
	v_lshlrev_b64 v[20:21], 10, v[20:21]
	v_lshl_add_u64 v[26:27], v[20:21], 0, v[16:17]
	s_mov_b32 s100, 0xb0000
	v_lshl_add_u64 v[234:235], v[250:251], 0, s[100:101]
	global_load_dwordx4 v[222:225], v[234:235], off offset:48
	global_load_dwordx4 v[226:229], v[234:235], off offset:32
	global_load_dwordx4 v[230:233], v[234:235], off offset:16
	s_nop 0
	global_load_dwordx4 v[234:237], v[234:235], off
	v_lshl_add_u64 v[26:27], v[26:27], 1, s[50:51]
	s_waitcnt vmcnt(15)
; #define LAS __attribute__((address_space(3)))
; __device__ __forceinline__ unsigned cvt_pk_bf16(float lo, float hi) { unsigned r; asm volatile("v_cvt_pk_bf16_f32 %0, %1, %2" : "=v"(r) : "v"(lo), "v"(hi)); return r; }
; __device__ __forceinline__ int lane_id() { return (int)__builtin_amdgcn_mbcnt_hi(~0u, __builtin_amdgcn_mbcnt_lo(~0u, 0u)); }
; #define PG8_BAR __builtin_amdgcn_s_barrier()
;     ...
;         { const int l2 = lane_id(); E(acc, cur, wr, wc, l2 & 15, l2 >> 4, rowtab + 512 * (ui % 3)); }
;         if (!has_next) break;
; #pragma unroll
;         for (int a = 0; a < 2; ++a)
; #pragma unroll
;             for (int b = 0; b < 2; ++b)
; #pragma unroll
;                 for (int m = 0; m < 4; ++m)
; #pragma unroll
;                     for (int n = 0; n < 2; ++n) acc[a][b][m][n] = (f32x4){0.f, 0.f, 0.f, 0.f};
;         cur = nxt; cB = nB; cA = nA; ++ui; fresh_cur = fresh_nxt;
;         if constexpr (GATHER) { const u32x4 _t = *(const LAS u32x4*)vnslot; vc[0][0] = _t.x; vc[0][1] = _t.y; vc[1][0] = _t.z; vc[1][1] = _t.w; }
;         if (wr == 1) PG8_BAR;
;     __device__ __forceinline__ void operator()(const f32x4 (&acc)[2][2][4][2], const Unit& u, int wr, int wc, int fr, int fq, const LAS unsigned* rt) const {
;     ...
;         for (int ai = 0; ai < 2; ++ai)
; #pragma unroll
;             for (int m = 0; m < 4; ++m) { const size_t o = (size_t)(u.pm * BM + ai * HALF + wr * 64 + m * 16 + fr) * D + col0;
;                 const f32x4 x0 = *(const f32x4*)(x + o), x1 = *(const f32x4*)(x + o + 4), x2 = *(const f32x4*)(x + o + 8), x3 = *(const f32x4*)(x + o + 12);
;                 const f32x4 xs[2][2] = {{x0, x1}, {x2, x3}};
; #pragma unroll
;                 for (int bj = 0; bj < 2; ++bj) {
;                     const f32x4 t0 = xs[bj][0] * ALPHA + g[bj][0] * acc[ai][bj][m][0], t1 = xs[bj][1] * ALPHA + g[bj][1] * acc[ai][bj][m][1];
;                     u32x4 w; w.x = cvt_pk_bf16(t0[0], t0[1]); w.y = cvt_pk_bf16(t0[2], t0[3]); w.z = cvt_pk_bf16(t1[0], t1[1]); w.w = cvt_pk_bf16(t1[2], t1[3]);
;                     *(u32x4*)(tb + o + 8 * bj) = w; } }
;     }
	v_pk_mul_f32 v[22:23], v[240:241], s[86:87] op_sel_hi:[1,0]
	v_pk_mul_f32 v[20:21], v[238:239], s[86:87] op_sel_hi:[1,0]
	s_waitcnt vmcnt(13)
	v_pk_mul_f32 v[86:87], v[248:249], s[86:87] op_sel_hi:[1,0]
	v_pk_mul_f32 v[84:85], v[246:247], s[86:87] op_sel_hi:[1,0]
	s_waitcnt vmcnt(12)
	v_pk_mul_f32 v[90:91], v[194:195], s[86:87] op_sel_hi:[1,0]
	v_pk_mul_f32 v[88:89], v[192:193], s[86:87] op_sel_hi:[1,0]
	v_pk_fma_f32 v[86:87], v[66:67], v[8:9], v[86:87]
	v_pk_fma_f32 v[66:67], v[64:65], v[10:11], v[84:85]
	v_pk_fma_f32 v[74:75], v[74:75], v[12:13], v[90:91]
	v_pk_fma_f32 v[72:73], v[72:73], v[14:15], v[88:89]
	v_pk_fma_f32 v[70:71], v[70:71], v[0:1], v[22:23]
	v_cvt_pk_bf16_f32 v64, v72, v73
	v_cvt_pk_bf16_f32 v65, v74, v75
	v_cvt_pk_bf16_f32 v66, v66, v67
	v_cvt_pk_bf16_f32 v67, v86, v87
	global_store_dwordx4 v[26:27], v[64:67], off
	v_pk_fma_f32 v[22:23], v[68:69], v[2:3], v[20:21]
	s_nop 0
	v_pk_mul_f32 v[66:67], v[242:243], s[86:87] op_sel_hi:[1,0]
	v_pk_mul_f32 v[64:65], v[244:245], s[86:87] op_sel_hi:[1,0]
	v_pk_fma_f32 v[66:67], v[76:77], v[6:7], v[66:67]
	v_pk_fma_f32 v[64:65], v[78:79], v[4:5], v[64:65]
	v_cvt_pk_bf16_f32 v20, v66, v67
	s_nop 0
	v_cvt_pk_bf16_f32 v21, v64, v65
	v_cvt_pk_bf16_f32 v22, v22, v23
	v_cvt_pk_bf16_f32 v23, v70, v71
	global_store_dwordx4 v[26:27], v[20:23], off offset:16
	s_nop 1
	v_add_u32_e32 v20, 0xa0, v18
	v_ashrrev_i32_e32 v21, 31, v20
	v_lshlrev_b64 v[20:21], 10, v[20:21]
	v_lshl_add_u64 v[26:27], v[20:21], 0, v[16:17]
	v_add_u32_e32 v18, 0xb0, v18
	v_lshl_add_u64 v[26:27], v[26:27], 1, s[50:51]
	v_ashrrev_i32_e32 v19, 31, v18
	v_lshlrev_b64 v[18:19], 10, v[18:19]
	s_waitcnt vmcnt(11)
	v_pk_mul_f32 v[22:23], v[208:209], s[86:87] op_sel_hi:[1,0]
	v_pk_mul_f32 v[20:21], v[206:207], s[86:87] op_sel_hi:[1,0]
	s_waitcnt vmcnt(9)
	v_pk_mul_f32 v[70:71], v[216:217], s[86:87] op_sel_hi:[1,0]
	v_pk_mul_f32 v[68:69], v[214:215], s[86:87] op_sel_hi:[1,0]
	s_waitcnt vmcnt(8)
	v_pk_mul_f32 v[74:75], v[220:221], s[86:87] op_sel_hi:[1,0]
	v_pk_mul_f32 v[72:73], v[218:219], s[86:87] op_sel_hi:[1,0]
	v_pk_fma_f32 v[70:71], v[50:51], v[8:9], v[70:71]
	v_pk_fma_f32 v[50:51], v[48:49], v[10:11], v[68:69]
	v_pk_fma_f32 v[58:59], v[58:59], v[12:13], v[74:75]
	v_pk_fma_f32 v[56:57], v[56:57], v[14:15], v[72:73]
	v_pk_fma_f32 v[54:55], v[54:55], v[0:1], v[22:23]
	v_cvt_pk_bf16_f32 v48, v56, v57
	v_cvt_pk_bf16_f32 v49, v58, v59
	v_cvt_pk_bf16_f32 v50, v50, v51
	v_cvt_pk_bf16_f32 v51, v70, v71
	global_store_dwordx4 v[26:27], v[48:51], off
	v_pk_fma_f32 v[22:23], v[52:53], v[2:3], v[20:21]
	s_nop 0
	v_pk_mul_f32 v[48:49], v[212:213], s[86:87] op_sel_hi:[1,0]
	v_pk_mul_f32 v[50:51], v[210:211], s[86:87] op_sel_hi:[1,0]
	v_pk_fma_f32 v[48:49], v[62:63], v[4:5], v[48:49]
	v_pk_fma_f32 v[50:51], v[60:61], v[6:7], v[50:51]
	s_nop 0
	v_cvt_pk_bf16_f32 v20, v50, v51
	v_cvt_pk_bf16_f32 v21, v48, v49
	v_cvt_pk_bf16_f32 v22, v22, v23
	v_cvt_pk_bf16_f32 v23, v54, v55
	global_store_dwordx4 v[26:27], v[20:23], off offset:16
	v_lshl_add_u64 v[26:27], v[18:19], 0, v[16:17]
	s_waitcnt vmcnt(4)
	v_pk_mul_f32 v[54:55], v[236:237], s[86:87] op_sel_hi:[1,0]
	v_pk_mul_f32 v[52:53], v[234:235], s[86:87] op_sel_hi:[1,0]
	v_pk_fma_f32 v[12:13], v[46:47], v[12:13], v[54:55]
	v_pk_mul_f32 v[46:47], v[230:231], s[86:87] op_sel_hi:[1,0]
	v_pk_fma_f32 v[14:15], v[44:45], v[14:15], v[52:53]
	v_pk_mul_f32 v[44:45], v[232:233], s[86:87] op_sel_hi:[1,0]
	v_pk_fma_f32 v[10:11], v[40:41], v[10:11], v[46:47]
	v_pk_fma_f32 v[42:43], v[42:43], v[8:9], v[44:45]
	v_cvt_pk_bf16_f32 v8, v14, v15
	v_cvt_pk_bf16_f32 v9, v12, v13
	v_cvt_pk_bf16_f32 v10, v10, v11
	v_lshl_add_u64 v[12:13], v[26:27], 1, s[50:51]
	v_cvt_pk_bf16_f32 v11, v42, v43
	global_store_dwordx4 v[12:13], v[8:11], off
	s_nop 1
	v_pk_mul_f32 v[10:11], v[226:227], s[86:87] op_sel_hi:[1,0]
	v_pk_mul_f32 v[8:9], v[228:229], s[86:87] op_sel_hi:[1,0]
	v_pk_fma_f32 v[6:7], v[36:37], v[6:7], v[10:11]
	v_pk_mul_f32 v[10:11], v[222:223], s[86:87] op_sel_hi:[1,0]
	v_pk_fma_f32 v[4:5], v[38:39], v[4:5], v[8:9]
	v_pk_mul_f32 v[8:9], v[224:225], s[86:87] op_sel_hi:[1,0]
	v_pk_fma_f32 v[2:3], v[32:33], v[2:3], v[10:11]
	v_pk_fma_f32 v[8:9], v[34:35], v[0:1], v[8:9]
	v_cvt_pk_bf16_f32 v0, v6, v7
	v_cvt_pk_bf16_f32 v1, v4, v5
	v_cvt_pk_bf16_f32 v2, v2, v3
	s_nop 0
	v_cvt_pk_bf16_f32 v3, v8, v9
	global_store_dwordx4 v[12:13], v[0:3], off offset:16
	s_cbranch_scc1 .LBB0_404
	s_and_b64 s[4:5], s[8:9], exec
	s_cselect_b32 s12, s64, s12
	s_andn2_b64 vcc, exec, s[10:11]
	s_cbranch_vccnz .LBB0_403
	s_barrier
	s_branch .LBB0_403
